# speedup vs baseline: 1.0123x; 1.0123x over previous
_Z9k4_reducePKjP15HIP_vector_typeIjLj2EE:
	s_load_dwordx4 s[4:7], s[0:1], 0x0
	s_cmp_ge_u32 s2, 0xc0
	s_cselect_b32 s8, 1, 0
	s_mul_i32 s9, s8, 0xc0
	s_sub_u32 s9, s2, s9
	s_lshl_b32 s9, s9, 8
	s_mul_i32 s10, s8, 0x600000
	s_add_u32 s9, s9, s10
	s_mov_b32 s11, 0x60000
	v_and_b32_e32 v1, 15, v0
	v_lshrrev_b32_e32 v2, 4, v0
	v_lshlrev_b32_e32 v3, 4, v1
	v_mad_u32_u24 v3, v2, s11, v3
	s_waitcnt lgkmcnt(0)
	s_add_u32 s12, s4, s9
	s_addc_u32 s13, s5, 0
	s_add_u32 s14, s12, 0xc000
	s_addc_u32 s15, s13, 0
	s_add_u32 s16, s14, 0xc000
	s_addc_u32 s17, s15, 0
	s_add_u32 s18, s16, 0xc000
	s_addc_u32 s19, s17, 0
	s_add_u32 s20, s18, 0xc000
	s_addc_u32 s21, s19, 0
	s_add_u32 s22, s20, 0xc000
	s_addc_u32 s23, s21, 0
	s_add_u32 s24, s22, 0xc000
	s_addc_u32 s25, s23, 0
	s_add_u32 s26, s24, 0xc000
	s_addc_u32 s27, s25, 0
	global_load_dwordx4 v[4:7], v3, s[12:13] nt
	global_load_dwordx4 v[8:11], v3, s[14:15] nt
	global_load_dwordx4 v[12:15], v3, s[16:17] nt
	global_load_dwordx4 v[16:19], v3, s[18:19] nt
	global_load_dwordx4 v[20:23], v3, s[20:21] nt
	global_load_dwordx4 v[24:27], v3, s[22:23] nt
	global_load_dwordx4 v[28:31], v3, s[24:25] nt
	global_load_dwordx4 v[32:35], v3, s[26:27] nt
	v_lshlrev_b32_e32 v36, 9, v2
	v_lshl_or_b32 v36, v1, 4, v36
	v_bfe_u32 v37, v0, 1, 1
	v_lshlrev_b32_e32 v37, 8, v37
	v_lshrrev_b32_e32 v48, 2, v0
	v_lshl_or_b32 v37, v48, 4, v37
	v_and_b32_e32 v48, 1, v0
	v_lshl_or_b32 v37, v48, 3, v37
	v_lshl_or_b32 v38, s2, 6, v0
	v_lshlrev_b32_e32 v38, 3, v38
	s_waitcnt vmcnt(7)
	v_lshrrev_b32_e32 v40, 16, v4
	v_and_b32_e32 v41, 0xffff, v4
	v_lshrrev_b32_e32 v42, 16, v5
	v_and_b32_e32 v43, 0xffff, v5
	v_lshrrev_b32_e32 v44, 16, v6
	v_and_b32_e32 v45, 0xffff, v6
	v_lshrrev_b32_e32 v46, 16, v7
	v_and_b32_e32 v47, 0xffff, v7
	s_waitcnt vmcnt(5)
	v_lshrrev_b32_e32 v48, 16, v8
	v_lshrrev_b32_e32 v49, 16, v12
	v_and_b32_e32 v50, 0xffff, v8
	v_and_b32_e32 v51, 0xffff, v12
	v_add3_u32 v40, v40, v48, v49
	v_add3_u32 v41, v41, v50, v51
	v_lshrrev_b32_e32 v48, 16, v9
	v_lshrrev_b32_e32 v49, 16, v13
	v_and_b32_e32 v50, 0xffff, v9
	v_and_b32_e32 v51, 0xffff, v13
	v_add3_u32 v42, v42, v48, v49
	v_add3_u32 v43, v43, v50, v51
	v_lshrrev_b32_e32 v48, 16, v10
	v_lshrrev_b32_e32 v49, 16, v14
	v_and_b32_e32 v50, 0xffff, v10
	v_and_b32_e32 v51, 0xffff, v14
	v_add3_u32 v44, v44, v48, v49
	v_add3_u32 v45, v45, v50, v51
	v_lshrrev_b32_e32 v48, 16, v11
	v_lshrrev_b32_e32 v49, 16, v15
	v_and_b32_e32 v50, 0xffff, v11
	v_and_b32_e32 v51, 0xffff, v15
	v_add3_u32 v46, v46, v48, v49
	v_add3_u32 v47, v47, v50, v51
	s_waitcnt vmcnt(3)
	v_lshrrev_b32_e32 v48, 16, v16
	v_lshrrev_b32_e32 v49, 16, v20
	v_and_b32_e32 v50, 0xffff, v16
	v_and_b32_e32 v51, 0xffff, v20
	v_add3_u32 v40, v40, v48, v49
	v_add3_u32 v41, v41, v50, v51
	v_lshrrev_b32_e32 v48, 16, v17
	v_lshrrev_b32_e32 v49, 16, v21
	v_and_b32_e32 v50, 0xffff, v17
	v_and_b32_e32 v51, 0xffff, v21
	v_add3_u32 v42, v42, v48, v49
	v_add3_u32 v43, v43, v50, v51
	v_lshrrev_b32_e32 v48, 16, v18
	v_lshrrev_b32_e32 v49, 16, v22
	v_and_b32_e32 v50, 0xffff, v18
	v_and_b32_e32 v51, 0xffff, v22
	v_add3_u32 v44, v44, v48, v49
	v_add3_u32 v45, v45, v50, v51
	v_lshrrev_b32_e32 v48, 16, v19
	v_lshrrev_b32_e32 v49, 16, v23
	v_and_b32_e32 v50, 0xffff, v19
	v_and_b32_e32 v51, 0xffff, v23
	v_add3_u32 v46, v46, v48, v49
	v_add3_u32 v47, v47, v50, v51
	s_waitcnt vmcnt(1)
	v_lshrrev_b32_e32 v48, 16, v24
	v_lshrrev_b32_e32 v49, 16, v28
	v_and_b32_e32 v50, 0xffff, v24
	v_and_b32_e32 v51, 0xffff, v28
	v_add3_u32 v40, v40, v48, v49
	v_add3_u32 v41, v41, v50, v51
	v_lshrrev_b32_e32 v48, 16, v25
	v_lshrrev_b32_e32 v49, 16, v29
	v_and_b32_e32 v50, 0xffff, v25
	v_and_b32_e32 v51, 0xffff, v29
	v_add3_u32 v42, v42, v48, v49
	v_add3_u32 v43, v43, v50, v51
	v_lshrrev_b32_e32 v48, 16, v26
	v_lshrrev_b32_e32 v49, 16, v30
	v_and_b32_e32 v50, 0xffff, v26
	v_and_b32_e32 v51, 0xffff, v30
	v_add3_u32 v44, v44, v48, v49
	v_add3_u32 v45, v45, v50, v51
	v_lshrrev_b32_e32 v48, 16, v27
	v_lshrrev_b32_e32 v49, 16, v31
	v_and_b32_e32 v50, 0xffff, v27
	v_and_b32_e32 v51, 0xffff, v31
	v_add3_u32 v46, v46, v48, v49
	v_add3_u32 v47, v47, v50, v51
	s_waitcnt vmcnt(0)
	v_lshrrev_b32_e32 v48, 16, v32
	v_and_b32_e32 v50, 0xffff, v32
	v_add_u32_e32 v40, v40, v48
	v_add_u32_e32 v41, v41, v50
	v_lshrrev_b32_e32 v48, 16, v33
	v_and_b32_e32 v50, 0xffff, v33
	v_add_u32_e32 v42, v42, v48
	v_add_u32_e32 v43, v43, v50
	v_lshrrev_b32_e32 v48, 16, v34
	v_and_b32_e32 v50, 0xffff, v34
	v_add_u32_e32 v44, v44, v48
	v_add_u32_e32 v45, v45, v50
	v_lshrrev_b32_e32 v48, 16, v35
	v_and_b32_e32 v50, 0xffff, v35
	v_add_u32_e32 v46, v46, v48
	v_add_u32_e32 v47, v47, v50
	ds_write_b128 v36, v[40:43]
	ds_write_b128 v36, v[44:47] offset:256
	v_cmp_gt_u32_e32 vcc, 64, v0
	s_waitcnt lgkmcnt(0)
	s_barrier
	s_and_saveexec_b64 s[0:1], vcc
	s_cbranch_execz .Lk4_end
	ds_read2st64_b64 v[4:7], v37 offset0:0 offset1:1
	ds_read2st64_b64 v[8:11], v37 offset0:2 offset1:3
	ds_read2st64_b64 v[12:15], v37 offset0:4 offset1:5
	ds_read2st64_b64 v[16:19], v37 offset0:6 offset1:7
	ds_read2st64_b64 v[20:23], v37 offset0:8 offset1:9
	ds_read2st64_b64 v[24:27], v37 offset0:10 offset1:11
	ds_read2st64_b64 v[28:31], v37 offset0:12 offset1:13
	ds_read2st64_b64 v[32:35], v37 offset0:14 offset1:15
	s_waitcnt lgkmcnt(6)
	v_add_u32_e32 v40, v4, v6
	v_add_u32_e32 v41, v5, v7
	v_add3_u32 v40, v40, v8, v10
	v_add3_u32 v41, v41, v9, v11
	s_waitcnt lgkmcnt(5)
	v_add3_u32 v40, v40, v12, v14
	v_add3_u32 v41, v41, v13, v15
	s_waitcnt lgkmcnt(4)
	v_add3_u32 v40, v40, v16, v18
	v_add3_u32 v41, v41, v17, v19
	s_waitcnt lgkmcnt(3)
	v_add3_u32 v40, v40, v20, v22
	v_add3_u32 v41, v41, v21, v23
	s_waitcnt lgkmcnt(2)
	v_add3_u32 v40, v40, v24, v26
	v_add3_u32 v41, v41, v25, v27
	s_waitcnt lgkmcnt(1)
	v_add3_u32 v40, v40, v28, v30
	v_add3_u32 v41, v41, v29, v31
	s_waitcnt lgkmcnt(0)
	v_add3_u32 v40, v40, v32, v34
	v_add3_u32 v41, v41, v33, v35
	global_store_dwordx2 v38, v[40:41], s[6:7]
